# baseline (speedup 1.0000x reference)
.LBB2_3:
	v_mfma_f32_32x32x16_f16 v[0:15], v[26:29], v[44:47], 0
	v_add_u32_e32 v108, s3, v104
	v_lshl_add_u32 v18, v108, 2, v106
	v_mbcnt_lo_u32_b32 v68, -1, 0
	v_mbcnt_hi_u32_b32 v68, -1, v68
	v_lshrrev_b32_e32 v68, 5, v68
	v_mad_u32_u24 v18, v68, 60, v18
	ds_read_b64 v[68:69], v18
	ds_read_b64 v[80:81], v18 offset:128
	ds_read_b64 v[76:77], v18 offset:256
	ds_read_b64 v[74:75], v18 offset:384
	ds_read_b64 v[86:87], v18 offset:512
	ds_read_b64 v[84:85], v18 offset:640
	ds_read_b64 v[82:83], v18 offset:768
	ds_read_b64 v[78:79], v18 offset:896
	s_nop 1
	v_exp_f32_e32 v16, v0
	v_exp_f32_e32 v17, v1
	s_nop 0
	v_pk_add_f32 v[66:67], v[16:17], 1.0 op_sel_hi:[1,0]
	v_mfma_f32_32x32x16_f16 v[16:31], v[26:29], v[32:35], 0
	v_log_f32_e32 v88, v66
	v_log_f32_e32 v89, v67
	v_exp_f32_e32 v66, v2
	v_exp_f32_e32 v67, v3
	s_waitcnt lgkmcnt(6)
	v_permlane32_swap_b32_e32 v68, v69
	v_permlane32_swap_b32_e32 v80, v81
	s_nop 0
	s_nop 6
	v_pk_mul_f32 v[94:95], v[80:81], v[18:19]
	v_exp_f32_e32 v18, v4
	v_exp_f32_e32 v19, v5
	s_waitcnt lgkmcnt(5)
	v_permlane32_swap_b32_e32 v76, v77
	s_nop 0
	v_pk_mul_f32 v[70:71], v[76:77], v[20:21]
	v_exp_f32_e32 v20, v6
	v_exp_f32_e32 v21, v7
	v_pk_mul_f32 v[100:101], v[68:69], v[16:17]
	v_pk_add_f32 v[16:17], v[66:67], 1.0 op_sel_hi:[1,0]
	v_pk_add_f32 v[18:19], v[18:19], 1.0 op_sel_hi:[1,0]
	v_log_f32_e32 v98, v16
	v_log_f32_e32 v99, v17
	v_log_f32_e32 v96, v18
	v_log_f32_e32 v97, v19
	v_pk_add_f32 v[18:19], v[20:21], 1.0 op_sel_hi:[1,0]
	v_pk_add_f32 v[16:17], v[88:89], 0 op_sel_hi:[1,0]
	v_log_f32_e32 v92, v18
	v_log_f32_e32 v93, v19
	v_pk_add_f32 v[16:17], v[98:99], v[16:17]
	v_exp_f32_e32 v18, v8
	v_pk_add_f32 v[16:17], v[96:97], v[16:17]
	v_exp_f32_e32 v19, v9
	v_pk_add_f32 v[66:67], v[92:93], v[16:17]
	v_exp_f32_e32 v16, v10
	v_exp_f32_e32 v17, v11
	v_pk_add_f32 v[18:19], v[18:19], 1.0 op_sel_hi:[1,0]
	s_waitcnt lgkmcnt(0)
	v_permlane32_swap_b32_e32 v74, v75
	v_permlane32_swap_b32_e32 v86, v87
	v_permlane32_swap_b32_e32 v84, v85
	v_permlane32_swap_b32_e32 v82, v83
	v_permlane32_swap_b32_e32 v78, v79
	s_nop 0
	v_pk_mul_f32 v[30:31], v[78:79], v[30:31]
	v_log_f32_e32 v90, v18
	v_log_f32_e32 v91, v19
	v_pk_add_f32 v[16:17], v[16:17], 1.0 op_sel_hi:[1,0]
	v_exp_f32_e32 v18, v12
	v_exp_f32_e32 v19, v13
	v_log_f32_e32 v20, v16
	v_log_f32_e32 v21, v17
	v_exp_f32_e32 v16, v14
	v_exp_f32_e32 v17, v15
	v_pk_add_f32 v[18:19], v[18:19], 1.0 op_sel_hi:[1,0]
	v_pk_add_f32 v[66:67], v[90:91], v[66:67]
	v_log_f32_e32 v18, v18
	v_log_f32_e32 v19, v19
	v_pk_add_f32 v[16:17], v[16:17], 1.0 op_sel_hi:[1,0]
	v_pk_add_f32 v[66:67], v[20:21], v[66:67]
	v_log_f32_e32 v16, v16
	v_log_f32_e32 v17, v17
	v_pk_add_f32 v[66:67], v[18:19], v[66:67]
	v_pk_mul_f32 v[28:29], v[82:83], v[28:29]
	v_pk_mul_f32 v[26:27], v[84:85], v[26:27]
	v_pk_add_f32 v[66:67], v[16:17], v[66:67]
	v_pk_mul_f32 v[24:25], v[86:87], v[24:25]
	v_add_f32_e32 v109, v66, v67
	v_pk_mul_f32 v[22:23], v[74:75], v[22:23]
	v_cmp_ngt_f32_e32 vcc, s10, v109
	s_cbranch_vccz .LBB2_5
	v_cmp_lt_f32_e32 vcc, s11, v1
	s_nop 1
	v_cndmask_b32_e32 v1, v89, v1, vcc
	v_mul_f32_e32 v66, v62, v1
	v_exp_f32_e32 v89, v66
	v_cmp_lt_f32_e32 vcc, s11, v0
	s_nop 1
	v_cndmask_b32_e32 v0, v88, v0, vcc
	v_cmp_lt_f32_e32 vcc, s11, v2
	v_pk_mul_f32 v[66:67], v[100:101], v[0:1]
	v_pk_add_f32 v[0:1], v[0:1], 0 op_sel_hi:[1,0]
	v_cndmask_b32_e32 v2, v98, v2, vcc
	v_cmp_lt_f32_e32 vcc, s11, v3
	v_fmac_f32_e32 v67, v89, v66
	s_nop 0
	v_cndmask_b32_e32 v3, v99, v3, vcc
	v_pk_mul_f32 v[88:89], v[62:63], v[2:3]
	v_cmp_lt_f32_e32 vcc, s11, v4
	v_exp_f32_e32 v66, v88
	v_exp_f32_e32 v98, v89
	v_pk_mul_f32 v[88:89], v[94:95], v[2:3]
	v_cndmask_b32_e32 v4, v96, v4, vcc
	v_cmp_lt_f32_e32 vcc, s11, v5
	v_fma_f32 v66, v66, v67, v88
	v_fmac_f32_e32 v89, v98, v66
	v_cndmask_b32_e32 v5, v97, v5, vcc
	v_pk_mul_f32 v[66:67], v[62:63], v[4:5]
	v_cmp_lt_f32_e32 vcc, s11, v6
	v_exp_f32_e32 v66, v66
	v_exp_f32_e32 v67, v67
	v_pk_add_f32 v[0:1], v[2:3], v[0:1]
	v_pk_mul_f32 v[2:3], v[70:71], v[4:5]
	v_cndmask_b32_e32 v6, v92, v6, vcc
	v_cmp_lt_f32_e32 vcc, s11, v7
	v_fma_f32 v2, v66, v89, v2
	v_fmac_f32_e32 v3, v67, v2
	v_cndmask_b32_e32 v7, v93, v7, vcc
	v_pk_mul_f32 v[66:67], v[62:63], v[6:7]
	v_pk_add_f32 v[0:1], v[4:5], v[0:1]
	v_exp_f32_e32 v2, v66
	v_exp_f32_e32 v66, v67
	v_pk_mul_f32 v[4:5], v[22:23], v[6:7]
	v_cmp_lt_f32_e32 vcc, s11, v8
	v_fma_f32 v2, v2, v3, v4
	v_fmac_f32_e32 v5, v66, v2
	v_cndmask_b32_e32 v2, v90, v8, vcc
	v_cmp_lt_f32_e32 vcc, s11, v9
	v_pk_add_f32 v[0:1], v[6:7], v[0:1]
	s_nop 0
	v_cndmask_b32_e32 v3, v91, v9, vcc
	v_pk_mul_f32 v[8:9], v[62:63], v[2:3]
	v_pk_mul_f32 v[6:7], v[24:25], v[2:3]
	v_exp_f32_e32 v4, v8
	v_exp_f32_e32 v8, v9
	v_cmp_lt_f32_e32 vcc, s11, v10
	v_pk_add_f32 v[0:1], v[2:3], v[0:1]
	v_fma_f32 v4, v4, v5, v6
	v_fmac_f32_e32 v7, v8, v4
	v_cndmask_b32_e32 v4, v20, v10, vcc
	v_cmp_lt_f32_e32 vcc, s11, v11
	s_nop 1
	v_cndmask_b32_e32 v5, v21, v11, vcc
	v_pk_mul_f32 v[8:9], v[62:63], v[4:5]
	v_pk_mul_f32 v[2:3], v[26:27], v[4:5]
	v_exp_f32_e32 v6, v8
	v_exp_f32_e32 v8, v9
	v_cmp_lt_f32_e32 vcc, s11, v12
	v_pk_add_f32 v[0:1], v[4:5], v[0:1]
	v_fma_f32 v2, v6, v7, v2
	v_cndmask_b32_e32 v6, v18, v12, vcc
	v_cmp_lt_f32_e32 vcc, s11, v13
	v_fmac_f32_e32 v3, v8, v2
	s_nop 0
	v_cndmask_b32_e32 v7, v19, v13, vcc
	v_pk_mul_f32 v[8:9], v[62:63], v[6:7]
	v_pk_mul_f32 v[4:5], v[28:29], v[6:7]
	v_exp_f32_e32 v2, v8
	v_exp_f32_e32 v8, v9
	v_cmp_lt_f32_e32 vcc, s11, v14
	v_pk_add_f32 v[0:1], v[6:7], v[0:1]
	v_fma_f32 v2, v2, v3, v4
	v_fmac_f32_e32 v5, v8, v2
	v_cndmask_b32_e32 v2, v16, v14, vcc
	v_cmp_lt_f32_e32 vcc, s11, v15
	s_nop 1
	v_cndmask_b32_e32 v3, v17, v15, vcc
	v_pk_mul_f32 v[8:9], v[62:63], v[2:3]
	v_pk_mul_f32 v[70:71], v[30:31], v[2:3]
	v_exp_f32_e32 v4, v8
	v_exp_f32_e32 v8, v9
	v_pk_add_f32 v[66:67], v[2:3], v[0:1]
	v_fma_f32 v4, v4, v5, v70
	v_fmac_f32_e32 v71, v8, v4
	s_branch .LBB2_6

.LBB3_3:
	s_waitcnt vmcnt(0)
	v_mfma_f32_32x32x16_f16 v[18:33], v[78:81], v[66:69], 0
	v_add_u32_e32 v149, s3, v89
	v_lshl_add_u32 v4, v149, 2, v147
	v_mbcnt_lo_u32_b32 v122, -1, 0
	v_mbcnt_hi_u32_b32 v122, -1, v122
	v_lshrrev_b32_e32 v122, 5, v122
	v_mad_u32_u24 v4, v122, 60, v4
	ds_read_b64 v[122:123], v4
	ds_read_b64 v[98:99], v4 offset:128
	ds_read_b64 v[100:101], v4 offset:256
	ds_read_b64 v[102:103], v4 offset:384
	ds_read_b64 v[104:105], v4 offset:512
	ds_read_b64 v[106:107], v4 offset:640
	ds_read_b64 v[110:111], v4 offset:896
	ds_read_b64 v[108:109], v4 offset:768
	s_nop 1
	v_exp_f32_e32 v2, v18
	v_exp_f32_e32 v3, v19
	v_mfma_f32_32x32x16_f16 v[34:49], v[78:81], v[54:57], 0
	v_exp_f32_e32 v120, v26
	v_exp_f32_e32 v121, v27
	v_pk_add_f32 v[2:3], v[2:3], 1.0 op_sel_hi:[1,0]
	v_exp_f32_e32 v126, v30
	v_log_f32_e32 v112, v2
	v_log_f32_e32 v113, v3
	v_exp_f32_e32 v127, v31
	s_waitcnt lgkmcnt(6)
	v_permlane32_swap_b32_e32 v122, v123
	v_permlane32_swap_b32_e32 v98, v99
	s_nop 0
	s_nop 3
	v_pk_mul_f32 v[36:37], v[98:99], v[36:37]
	s_waitcnt lgkmcnt(5)
	v_permlane32_swap_b32_e32 v100, v101
	s_nop 0
	v_pk_mul_f32 v[38:39], v[100:101], v[38:39]
	v_pk_mul_f32 v[2:3], v[96:97], v[112:113]
	s_waitcnt lgkmcnt(4)
	v_permlane32_swap_b32_e32 v102, v103
	s_nop 0
	v_pk_mul_f32 v[40:41], v[102:103], v[40:41]
	v_exp_f32_e32 v114, v2
	v_exp_f32_e32 v115, v3
	v_mfma_f32_32x32x16_f16 v[2:17], v[78:81], v[50:53], 0
	v_exp_f32_e32 v80, v20
	v_exp_f32_e32 v81, v21
	v_pk_mul_f32 v[78:79], v[122:123], v[34:35]
	s_waitcnt lgkmcnt(3)
	v_permlane32_swap_b32_e32 v104, v105
	s_nop 0
	v_pk_mul_f32 v[42:43], v[104:105], v[42:43]
	v_pk_mul_f32 v[118:119], v[78:79], v[112:113]
	v_pk_add_f32 v[34:35], v[80:81], 1.0 op_sel_hi:[1,0]
	v_fma_mix_f32 v118, v114, v151, v118 op_sel_hi:[0,1,0]
	v_log_f32_e32 v34, v34
	v_log_f32_e32 v35, v35
	v_fmac_f32_e32 v119, v115, v118
	v_exp_f32_e32 v114, v22
	v_exp_f32_e32 v115, v23
	v_pk_mul_f32 v[80:81], v[96:97], v[34:35]
	v_pk_mul_f32 v[128:129], v[36:37], v[34:35]
	v_exp_f32_e32 v80, v80
	v_exp_f32_e32 v116, v81
	s_waitcnt lgkmcnt(2)
	v_permlane32_swap_b32_e32 v106, v107
	s_nop 0
	v_pk_mul_f32 v[44:45], v[106:107], v[44:45]
	s_waitcnt lgkmcnt(0)
	v_permlane32_swap_b32_e32 v110, v111
	v_permlane32_swap_b32_e32 v108, v109
	s_nop 0
	v_pk_mul_f32 v[46:47], v[108:109], v[46:47]
	v_fma_f32 v128, v80, v119, v128
	v_pk_add_f32 v[80:81], v[114:115], 1.0 op_sel_hi:[1,0]
	v_exp_f32_e32 v114, v24
	v_log_f32_e32 v80, v80
	v_log_f32_e32 v81, v81
	v_exp_f32_e32 v115, v25
	v_fmac_f32_e32 v129, v116, v128
	v_pk_mul_f32 v[48:49], v[110:111], v[48:49]
	v_pk_mul_f32 v[116:117], v[96:97], v[80:81]
	v_pk_add_f32 v[114:115], v[114:115], 1.0 op_sel_hi:[1,0]
	v_exp_f32_e32 v116, v116
	v_exp_f32_e32 v117, v117
	v_log_f32_e32 v114, v114
	v_log_f32_e32 v115, v115
	v_pk_mul_f32 v[130:131], v[38:39], v[80:81]
	v_pk_mul_f32 v[132:133], v[40:41], v[114:115]
	v_fma_f32 v130, v116, v129, v130
	v_fmac_f32_e32 v131, v117, v130
	v_pk_mul_f32 v[116:117], v[96:97], v[114:115]
	s_nop 0
	v_exp_f32_e32 v116, v116
	v_exp_f32_e32 v124, v117
	v_fma_f32 v132, v116, v131, v132
	v_pk_add_f32 v[116:117], v[120:121], 1.0 op_sel_hi:[1,0]
	v_exp_f32_e32 v120, v28
	v_log_f32_e32 v116, v116
	v_log_f32_e32 v117, v117
	v_exp_f32_e32 v121, v29
	v_fmac_f32_e32 v133, v124, v132
	v_pk_mul_f32 v[124:125], v[96:97], v[116:117]
	s_nop 0
	v_exp_f32_e32 v124, v124
	v_pk_add_f32 v[120:121], v[120:121], 1.0 op_sel_hi:[1,0]
	v_exp_f32_e32 v125, v125
	v_log_f32_e32 v120, v120
	v_log_f32_e32 v121, v121
	v_pk_mul_f32 v[134:135], v[42:43], v[116:117]
	v_pk_mul_f32 v[136:137], v[44:45], v[120:121]
	v_fma_f32 v134, v124, v133, v134
	v_fmac_f32_e32 v135, v125, v134
	v_pk_mul_f32 v[124:125], v[96:97], v[120:121]
	s_nop 0
	v_exp_f32_e32 v124, v124
	v_exp_f32_e32 v138, v125
	v_fma_f32 v136, v124, v135, v136
	v_pk_add_f32 v[124:125], v[126:127], 1.0 op_sel_hi:[1,0]
	v_exp_f32_e32 v126, v32
	v_log_f32_e32 v124, v124
	v_log_f32_e32 v125, v125
	v_exp_f32_e32 v127, v33
	v_fmac_f32_e32 v137, v138, v136
	v_pk_mul_f32 v[138:139], v[96:97], v[124:125]
	v_pk_add_f32 v[126:127], v[126:127], 1.0 op_sel_hi:[1,0]
	v_exp_f32_e32 v140, v138
	v_log_f32_e32 v126, v126
	v_log_f32_e32 v127, v127
	v_exp_f32_e32 v152, v139
	v_pk_mul_f32 v[138:139], v[46:47], v[124:125]
	s_nop 0
	v_fma_f32 v138, v140, v137, v138
	v_pk_mul_f32 v[140:141], v[96:97], v[126:127]
	v_fmac_f32_e32 v139, v152, v138
	v_exp_f32_e32 v153, v140
	v_exp_f32_e32 v154, v141
	v_pk_mul_f32 v[140:141], v[48:49], v[126:127]
	s_nop 0
	v_fma_f32 v140, v153, v139, v140
	v_fmac_f32_e32 v141, v154, v140
	v_cmp_nlt_f32_e64 vcc, |v141|, s10
	s_cbranch_vccz .LBB3_5
	v_cmp_lt_f32_e32 vcc, s11, v18
	v_cvt_f32_f16_e32 v118, v151
	s_nop 0
	v_cndmask_b32_e32 v18, v112, v18, vcc
	v_cmp_lt_f32_e32 vcc, s11, v19
	s_nop 1
	v_cndmask_b32_e32 v19, v113, v19, vcc
	v_pk_mul_f32 v[112:113], v[96:97], v[18:19]
	v_cmp_lt_f32_e32 vcc, s11, v20
	v_exp_f32_e32 v112, v112
	v_exp_f32_e32 v113, v113
	v_cndmask_b32_e32 v20, v34, v20, vcc
	v_cmp_lt_f32_e32 vcc, s11, v21
	v_pk_mul_f32 v[18:19], v[78:79], v[18:19]
	s_nop 0
	v_cndmask_b32_e32 v21, v35, v21, vcc
	v_pk_mul_f32 v[34:35], v[96:97], v[20:21]
	v_fma_f32 v18, v112, v118, v18
	v_exp_f32_e32 v34, v34
	v_fmac_f32_e32 v19, v113, v18
	v_cmp_lt_f32_e32 vcc, s11, v22
	v_pk_mul_f32 v[78:79], v[2:3], v[18:19]
	v_pk_mul_f32 v[2:3], v[36:37], v[20:21]
	v_cndmask_b32_e32 v18, v80, v22, vcc
	v_cmp_lt_f32_e32 vcc, s11, v23
	v_exp_f32_e32 v35, v35
	v_fma_f32 v2, v34, v19, v2
	v_cndmask_b32_e32 v19, v81, v23, vcc
	v_pk_mul_f32 v[20:21], v[96:97], v[18:19]
	v_fmac_f32_e32 v3, v35, v2
	v_exp_f32_e32 v20, v20
	v_cmp_lt_f32_e32 vcc, s11, v24
	v_pk_mul_f32 v[80:81], v[4:5], v[2:3]
	v_pk_mul_f32 v[4:5], v[38:39], v[18:19]
	v_cndmask_b32_e32 v2, v114, v24, vcc
	v_cmp_lt_f32_e32 vcc, s11, v25
	v_exp_f32_e32 v21, v21
	v_fma_f32 v4, v20, v3, v4
	v_cndmask_b32_e32 v3, v115, v25, vcc
	v_pk_mul_f32 v[18:19], v[96:97], v[2:3]
	v_fmac_f32_e32 v5, v21, v4
	v_exp_f32_e32 v18, v18
	v_cmp_lt_f32_e32 vcc, s11, v26
	v_pk_mul_f32 v[112:113], v[6:7], v[4:5]
	v_pk_mul_f32 v[2:3], v[40:41], v[2:3]
	v_cndmask_b32_e32 v4, v116, v26, vcc
	v_cmp_lt_f32_e32 vcc, s11, v27
	v_exp_f32_e32 v19, v19
	v_fma_f32 v2, v18, v5, v2
	v_cndmask_b32_e32 v5, v117, v27, vcc
	v_pk_mul_f32 v[6:7], v[96:97], v[4:5]
	v_fmac_f32_e32 v3, v19, v2
	v_exp_f32_e32 v6, v6
	v_exp_f32_e32 v7, v7
	v_cmp_lt_f32_e32 vcc, s11, v28
	v_pk_mul_f32 v[114:115], v[8:9], v[2:3]
	v_pk_mul_f32 v[4:5], v[42:43], v[4:5]
	v_cndmask_b32_e32 v2, v120, v28, vcc
	v_cmp_lt_f32_e32 vcc, s11, v29
	v_fma_f32 v4, v6, v3, v4
	v_fmac_f32_e32 v5, v7, v4
	v_cndmask_b32_e32 v3, v121, v29, vcc
	v_pk_mul_f32 v[6:7], v[96:97], v[2:3]
	v_cmp_lt_f32_e32 vcc, s11, v30
	v_exp_f32_e32 v6, v6
	v_exp_f32_e32 v7, v7
	v_pk_mul_f32 v[116:117], v[10:11], v[4:5]
	v_pk_mul_f32 v[2:3], v[44:45], v[2:3]
	v_cndmask_b32_e32 v4, v124, v30, vcc
	v_cmp_lt_f32_e32 vcc, s11, v31
	v_fma_f32 v2, v6, v5, v2
	v_fmac_f32_e32 v3, v7, v2
	v_cndmask_b32_e32 v5, v125, v31, vcc
	v_pk_mul_f32 v[6:7], v[96:97], v[4:5]
	v_cmp_lt_f32_e32 vcc, s11, v32
	v_exp_f32_e32 v6, v6
	v_exp_f32_e32 v7, v7
	v_pk_mul_f32 v[118:119], v[12:13], v[2:3]
	v_pk_mul_f32 v[4:5], v[46:47], v[4:5]
	v_cndmask_b32_e32 v2, v126, v32, vcc
	v_cmp_lt_f32_e32 vcc, s11, v33
	v_fma_f32 v4, v6, v3, v4
	v_fmac_f32_e32 v5, v7, v4
	v_cndmask_b32_e32 v3, v127, v33, vcc
	v_pk_mul_f32 v[6:7], v[96:97], v[2:3]
	v_pk_mul_f32 v[2:3], v[48:49], v[2:3]
	v_exp_f32_e32 v6, v6
	v_exp_f32_e32 v7, v7
	v_pk_mul_f32 v[120:121], v[14:15], v[4:5]
	v_fma_f32 v2, v6, v5, v2
	v_fmac_f32_e32 v3, v7, v2
	v_pk_mul_f32 v[124:125], v[16:17], v[2:3]
	s_branch .LBB3_6
